# retention score accumulators kept in arch VGPRs (no AGPR read-back); wconv at 88 VGPRs
# speedup vs baseline: 1.0366x; 1.0037x over previous
.Lwc_work:
	s_load_dword s8, s[0:1], 0x150
	s_cmp_eq_u32 s3, 5
	s_cselect_b32 s9, 13, 11
	s_cmp_eq_u32 s3, 6
	s_cselect_b32 s10, 13, 11
	s_sub_u32 s11, s9, 7
	s_lshr_b32 s12, s4, s11
	s_lshl_b32 s13, s12, s11
	s_sub_u32 s13, s4, s13
	s_add_u32 s20, s9, 2
	s_add_u32 s21, s10, 1
	v_lshrrev_b32_e32 v4, 5, v0
	v_and_b32_e32 v6, 31, v0
	v_lshlrev_b32_e32 v5, 4, v4
	v_lshlrev_b32_e32 v5, s20, v5
	v_lshl_add_u32 v1, v6, 4, v5
	v_lshlrev_b32_e32 v7, 1, v4
	v_and_b32_e32 v8, 7, v6
	v_xor_b32_e32 v7, v7, v8
	v_lshlrev_b32_e32 v7, 4, v7
	v_lshl_add_u32 v2, v6, 10, v7
	v_xor_b32_e32 v3, 16, v2
	v_lshrrev_b32_e32 v9, 4, v0
	v_and_b32_e32 v10, 15, v0
	v_lshrrev_b32_e32 v11, 6, v0
	v_xor_b32_e32 v11, v10, v11
	v_lshlrev_b32_e32 v11, 4, v11
	v_lshl_add_u32 v84, v9, 8, v11
	v_xor_b32_e32 v85, 64, v84
	v_lshlrev_b32_e32 v12, s21, v9
	v_lshl_add_u32 v86, v10, 4, v12
	s_add_u32 s22, s20, 7
	s_lshl_b32 s23, s12, s22
	s_lshl_b32 s24, s13, 9
	s_add_u32 s23, s23, s24
	s_lshl_b32 s25, 1, s20
	s_add_u32 s26, s21, 7
	s_lshl_b32 s27, s13, s26
	s_lshl_b32 s28, s12, 8
	s_add_u32 s27, s27, s28
	s_add_u32 s29, s10, 5
	s_lshl_b32 s29, 1, s29
	s_waitcnt lgkmcnt(0)
	s_add_u32 s8, s8, s3
	s_lshl_b32 s8, s8, 3
	s_add_u32 s14, s0, s8
	s_addc_u32 s15, s1, 0
	s_load_dwordx2 s[16:17], s[14:15], 0x0
	s_load_dwordx2 s[18:19], s[14:15], 0x70
	s_waitcnt lgkmcnt(0)
	s_add_u32 s16, s16, s23
	s_addc_u32 s17, s17, 0
	s_add_u32 s18, s18, s27
	s_addc_u32 s19, s19, 0
	global_load_dwordx4 v[4:7], v1, s[16:17] nt
	s_add_u32 s16, s16, s25
	s_addc_u32 s17, s17, 0
	global_load_dwordx4 v[8:11], v1, s[16:17] nt
	s_add_u32 s16, s16, s25
	s_addc_u32 s17, s17, 0
	global_load_dwordx4 v[12:15], v1, s[16:17] nt
	s_add_u32 s16, s16, s25
	s_addc_u32 s17, s17, 0
	global_load_dwordx4 v[16:19], v1, s[16:17] nt
	s_add_u32 s16, s16, s25
	s_addc_u32 s17, s17, 0
	global_load_dwordx4 v[20:23], v1, s[16:17] nt
	s_add_u32 s16, s16, s25
	s_addc_u32 s17, s17, 0
	global_load_dwordx4 v[24:27], v1, s[16:17] nt
	s_add_u32 s16, s16, s25
	s_addc_u32 s17, s17, 0
	global_load_dwordx4 v[28:31], v1, s[16:17] nt
	s_add_u32 s16, s16, s25
	s_addc_u32 s17, s17, 0
	global_load_dwordx4 v[32:35], v1, s[16:17] nt
	s_add_u32 s16, s16, s25
	s_addc_u32 s17, s17, 0
	global_load_dwordx4 v[36:39], v1, s[16:17] nt
	s_add_u32 s16, s16, s25
	s_addc_u32 s17, s17, 0
	global_load_dwordx4 v[40:43], v1, s[16:17] nt
	s_add_u32 s16, s16, s25
	s_addc_u32 s17, s17, 0
	global_load_dwordx4 v[44:47], v1, s[16:17] nt
	s_add_u32 s16, s16, s25
	s_addc_u32 s17, s17, 0
	global_load_dwordx4 v[48:51], v1, s[16:17] nt
	s_add_u32 s16, s16, s25
	s_addc_u32 s17, s17, 0
	global_load_dwordx4 v[52:55], v1, s[16:17] nt
	s_add_u32 s16, s16, s25
	s_addc_u32 s17, s17, 0
	global_load_dwordx4 v[56:59], v1, s[16:17] nt
	s_add_u32 s16, s16, s25
	s_addc_u32 s17, s17, 0
	global_load_dwordx4 v[60:63], v1, s[16:17] nt
	s_add_u32 s16, s16, s25
	s_addc_u32 s17, s17, 0
	global_load_dwordx4 v[64:67], v1, s[16:17] nt
	s_waitcnt vmcnt(14)
	v_cvt_pk_f16_f32 v68, v4, v8
	v_cvt_pk_f16_f32 v72, v5, v9
	v_cvt_pk_f16_f32 v76, v6, v10
	v_cvt_pk_f16_f32 v80, v7, v11
	s_waitcnt vmcnt(12)
	v_cvt_pk_f16_f32 v69, v12, v16
	v_cvt_pk_f16_f32 v73, v13, v17
	v_cvt_pk_f16_f32 v77, v14, v18
	v_cvt_pk_f16_f32 v81, v15, v19
	s_waitcnt vmcnt(10)
	v_cvt_pk_f16_f32 v70, v20, v24
	v_cvt_pk_f16_f32 v74, v21, v25
	v_cvt_pk_f16_f32 v78, v22, v26
	v_cvt_pk_f16_f32 v82, v23, v27
	s_waitcnt vmcnt(8)
	v_cvt_pk_f16_f32 v71, v28, v32
	v_cvt_pk_f16_f32 v75, v29, v33
	v_cvt_pk_f16_f32 v79, v30, v34
	v_cvt_pk_f16_f32 v83, v31, v35
	ds_write_b128 v2, v[68:71]
	ds_write_b128 v2, v[72:75] offset:256
	ds_write_b128 v2, v[76:79] offset:512
	ds_write_b128 v2, v[80:83] offset:768
	s_waitcnt vmcnt(6)
	v_cvt_pk_f16_f32 v4, v36, v40
	v_cvt_pk_f16_f32 v8, v37, v41
	v_cvt_pk_f16_f32 v12, v38, v42
	v_cvt_pk_f16_f32 v16, v39, v43
	s_waitcnt vmcnt(4)
	v_cvt_pk_f16_f32 v5, v44, v48
	v_cvt_pk_f16_f32 v9, v45, v49
	v_cvt_pk_f16_f32 v13, v46, v50
	v_cvt_pk_f16_f32 v17, v47, v51
	s_waitcnt vmcnt(2)
	v_cvt_pk_f16_f32 v6, v52, v56
	v_cvt_pk_f16_f32 v10, v53, v57
	v_cvt_pk_f16_f32 v14, v54, v58
	v_cvt_pk_f16_f32 v18, v55, v59
	s_waitcnt vmcnt(0)
	v_cvt_pk_f16_f32 v7, v60, v64
	v_cvt_pk_f16_f32 v11, v61, v65
	v_cvt_pk_f16_f32 v15, v62, v66
	v_cvt_pk_f16_f32 v19, v63, v67
	ds_write_b128 v3, v[4:7]
	ds_write_b128 v3, v[8:11] offset:256
	ds_write_b128 v3, v[12:15] offset:512
	ds_write_b128 v3, v[16:19] offset:768
	s_waitcnt lgkmcnt(0)
	s_barrier
	ds_read_b128 v[4:7], v84
	ds_read_b128 v[8:11], v85 offset:4096
	ds_read_b128 v[12:15], v84 offset:8192
	ds_read_b128 v[16:19], v85 offset:12288
	ds_read_b128 v[20:23], v84 offset:16384
	ds_read_b128 v[24:27], v85 offset:20480
	ds_read_b128 v[28:31], v84 offset:24576
	ds_read_b128 v[32:35], v85 offset:28672
	s_waitcnt lgkmcnt(7)
	global_store_dwordx4 v86, v[4:7], s[18:19] sc1
	s_add_u32 s18, s18, s29
	s_addc_u32 s19, s19, 0
	s_waitcnt lgkmcnt(6)
	global_store_dwordx4 v86, v[8:11], s[18:19] sc1
	s_add_u32 s18, s18, s29
	s_addc_u32 s19, s19, 0
	s_waitcnt lgkmcnt(5)
	global_store_dwordx4 v86, v[12:15], s[18:19] sc1
	s_add_u32 s18, s18, s29
	s_addc_u32 s19, s19, 0
	s_waitcnt lgkmcnt(4)
	global_store_dwordx4 v86, v[16:19], s[18:19] sc1
	s_add_u32 s18, s18, s29
	s_addc_u32 s19, s19, 0
	s_waitcnt lgkmcnt(3)
	global_store_dwordx4 v86, v[20:23], s[18:19] sc1
	s_add_u32 s18, s18, s29
	s_addc_u32 s19, s19, 0
	s_waitcnt lgkmcnt(2)
	global_store_dwordx4 v86, v[24:27], s[18:19] sc1
	s_add_u32 s18, s18, s29
	s_addc_u32 s19, s19, 0
	s_waitcnt lgkmcnt(1)
	global_store_dwordx4 v86, v[28:31], s[18:19] sc1
	s_add_u32 s18, s18, s29
	s_addc_u32 s19, s19, 0
	s_waitcnt lgkmcnt(0)
	global_store_dwordx4 v86, v[32:35], s[18:19] sc1

	.amdhsa_kernel _Z12wconv_kernel5WDesci
		.amdhsa_group_segment_fixed_size 32768
		.amdhsa_private_segment_fixed_size 0
		.amdhsa_kernarg_size 340
		.amdhsa_user_sgpr_count 2
		.amdhsa_user_sgpr_dispatch_ptr 0
		.amdhsa_user_sgpr_queue_ptr 0
		.amdhsa_user_sgpr_kernarg_segment_ptr 1
		.amdhsa_user_sgpr_dispatch_id 0
		.amdhsa_user_sgpr_kernarg_preload_length 0
		.amdhsa_user_sgpr_kernarg_preload_offset 0
		.amdhsa_user_sgpr_private_segment_size 0
		.amdhsa_uses_dynamic_stack 0
		.amdhsa_enable_private_segment 0
		.amdhsa_system_sgpr_workgroup_id_x 1
		.amdhsa_system_sgpr_workgroup_id_y 1
		.amdhsa_system_sgpr_workgroup_id_z 0
		.amdhsa_system_sgpr_workgroup_info 0
		.amdhsa_system_vgpr_workitem_id 0
		.amdhsa_next_free_vgpr 87
		.amdhsa_next_free_sgpr 30
		.amdhsa_accum_offset 88
		.amdhsa_reserve_vcc 0
		.amdhsa_float_round_mode_32 0
		.amdhsa_float_round_mode_16_64 0
		.amdhsa_float_denorm_mode_32 3
		.amdhsa_float_denorm_mode_16_64 3
		.amdhsa_dx10_clamp 1
		.amdhsa_ieee_mode 1
		.amdhsa_fp16_overflow 0
		.amdhsa_tg_split 0
		.amdhsa_exception_fp_ieee_invalid_op 0
		.amdhsa_exception_fp_denorm_src 0
		.amdhsa_exception_fp_ieee_div_zero 0
		.amdhsa_exception_fp_ieee_overflow 0
		.amdhsa_exception_fp_ieee_underflow 0
		.amdhsa_exception_fp_ieee_inexact 0
		.amdhsa_exception_int_div_zero 0
	.end_amdhsa_kernel

.LBB1_8:
	v_add_u32_e32 v159, s76, v148
	ds_read_b128 v[90:93], v159 offset:0
	s_waitcnt lgkmcnt(4)
	s_add_u32 s68, s52, s68
	s_addc_u32 s69, s53, s69
	v_mfma_f32_32x32x16_f16 v[188:203], v[78:81], v[2:5], 0
	s_and_b64 vcc, exec, s[0:1]
	v_lshl_add_u64 v[134:135], s[68:69], 0, v[94:95]
	s_cbranch_vccnz .LBB1_10
	s_add_i32 s78, s73, s77
	s_add_i32 m0, s78, 0x8000
	s_nop 0
	global_load_lds_dwordx4 v[134:135], off
.LBB1_10:
	v_add_u32_e32 v161, s76, v149
	ds_read_b128 v[78:81], v161 offset:0
	s_waitcnt lgkmcnt(4)
	v_mfma_f32_32x32x16_f16 v[204:219], v[74:77], v[6:9], 0
	s_and_b64 vcc, exec, s[0:1]
	v_lshl_add_u64 v[132:133], s[68:69], 0, v[96:97]
	s_cbranch_vccnz .LBB1_12
	s_add_i32 s68, s73, s77
	v_lshl_add_u64 v[74:75], v[132:133], 0, s[54:55]
	s_add_i32 m0, s68, 0x8400
	s_nop 0
	global_load_lds_dwordx4 v[74:75], off
.LBB1_12:
	v_add_u32_e32 v163, s76, v150
	ds_read_b128 v[82:85], v163 offset:0
	s_waitcnt lgkmcnt(4)
	v_mfma_f32_32x32x16_f16 v[188:203], v[70:73], v[10:13], v[188:203]
	s_and_b64 vcc, exec, s[0:1]
	s_cbranch_vccnz .LBB1_14
	s_add_i32 s68, s73, s77
	v_lshl_add_u64 v[70:71], v[134:135], 0, s[56:57]
	s_add_i32 m0, s68, 0x8800
	s_nop 0
	global_load_lds_dwordx4 v[70:71], off
.LBB1_14:
	v_add_u32_e32 v164, s76, v151
	ds_read_b128 v[86:89], v164 offset:0
	s_waitcnt lgkmcnt(4)
	v_mfma_f32_32x32x16_f16 v[204:219], v[66:69], v[14:17], v[204:219]
	s_and_b64 vcc, exec, s[0:1]
	s_cbranch_vccnz .LBB1_16
	s_add_i32 s68, s73, s77
	v_lshl_add_u64 v[66:67], v[132:133], 0, s[58:59]
	s_add_i32 m0, s68, 0x8c00
	s_nop 0
	global_load_lds_dwordx4 v[66:67], off
.LBB1_16:
	ds_read_b128 v[66:69], v165 offset:0x100
	s_waitcnt lgkmcnt(4)
	v_mfma_f32_32x32x16_f16 v[188:203], v[90:93], v[18:21], v[188:203]
	s_and_b64 vcc, exec, s[0:1]
	s_cbranch_vccnz .LBB1_18
	s_add_i32 s68, s73, s77
	v_lshl_add_u64 v[70:71], v[134:135], 0, s[60:61]
	s_add_i32 m0, s68, 0x9000
	s_nop 0
	global_load_lds_dwordx4 v[70:71], off
.LBB1_18:
	ds_read_b128 v[70:73], v162 offset:0x100
	s_waitcnt lgkmcnt(4)
	v_mfma_f32_32x32x16_f16 v[204:219], v[78:81], v[22:25], v[204:219]
	s_and_b64 vcc, exec, s[0:1]
	s_cbranch_vccnz .LBB1_20
	s_add_i32 s68, s73, s77
	v_lshl_add_u64 v[74:75], v[132:133], 0, s[62:63]
	s_add_i32 m0, s68, 0x9400
	s_nop 0
	global_load_lds_dwordx4 v[74:75], off
.LBB1_20:
	ds_read_b128 v[74:77], v160 offset:0x100
	s_waitcnt lgkmcnt(4)
	v_mfma_f32_32x32x16_f16 v[188:203], v[82:85], v[26:29], v[188:203]
	s_and_b64 vcc, exec, s[0:1]
	s_cbranch_vccnz .LBB1_22
	s_add_i32 s68, s73, s77
	v_lshl_add_u64 v[78:79], v[134:135], 0, s[64:65]
	s_add_i32 m0, s68, 0x9800
	s_nop 0
	global_load_lds_dwordx4 v[78:79], off
.LBB1_22:
	ds_read_b128 v[78:81], v158 offset:0x100
	s_waitcnt lgkmcnt(4)
	v_mfma_f32_32x32x16_f16 v[204:219], v[86:89], v[30:33], v[204:219]
	s_and_b64 vcc, exec, s[0:1]
	s_cbranch_vccnz .LBB1_24
	s_add_i32 s0, s73, s77
	v_lshl_add_u64 v[82:83], v[132:133], 0, s[66:67]
	s_add_i32 m0, s0, 0x9c00
	s_nop 0
	global_load_lds_dwordx4 v[82:83], off
.LBB1_24:
	v_cvt_f32_u32_e32 v82, v157
	v_mul_f32_e32 v82, v142, v82
	v_exp_f32_e32 v82, v82
	s_nop 0
	v_pk_mul_f32 v[90:91], v[100:101], v[82:83] op_sel_hi:[1,0]
	v_pk_mul_f32 v[92:93], v[102:103], v[82:83] op_sel_hi:[1,0]
	v_pk_mul_f32 v[132:133], v[104:105], v[82:83] op_sel_hi:[1,0]
	v_pk_mul_f32 v[134:135], v[106:107], v[82:83] op_sel_hi:[1,0]
	v_pk_mul_f32 v[86:87], v[110:111], v[82:83] op_sel_hi:[1,0]
	v_pk_mul_f32 v[88:89], v[112:113], v[82:83] op_sel_hi:[1,0]
	v_pk_mul_f32 v[166:167], v[108:109], v[82:83] op_sel_hi:[1,0]
	v_pk_mul_f32 v[168:169], v[98:99], v[82:83] op_sel_hi:[1,0]
	ds_read_b128 v[82:85], v159 offset:0x100
	s_waitcnt lgkmcnt(4)
	v_mfma_f32_32x32x16_f16 v[188:203], v[66:69], v[34:37], v[188:203]
	ds_read_b128 v[66:69], v161 offset:0x100
	s_waitcnt lgkmcnt(4)
	v_mfma_f32_32x32x16_f16 v[204:219], v[70:73], v[38:41], v[204:219]
	ds_read_b128 v[70:73], v163 offset:0x100
	s_waitcnt lgkmcnt(4)
	v_mfma_f32_32x32x16_f16 v[188:203], v[74:77], v[42:45], v[188:203]
	ds_read_b128 v[74:77], v164 offset:0x100
	s_waitcnt lgkmcnt(4)
	v_mfma_f32_32x32x16_f16 v[204:219], v[78:81], v[46:49], v[204:219]
	s_waitcnt lgkmcnt(3)
	v_mfma_f32_32x32x16_f16 v[188:203], v[82:85], v[50:53], v[188:203]
	s_waitcnt lgkmcnt(2)
	v_mfma_f32_32x32x16_f16 v[204:219], v[66:69], v[54:57], v[204:219]
	s_waitcnt lgkmcnt(1)
	v_mfma_f32_32x32x16_f16 v[188:203], v[70:73], v[58:61], v[188:203]
	s_waitcnt lgkmcnt(0)
	v_mfma_f32_32x32x16_f16 v[204:219], v[74:77], v[62:65], v[204:219]
	s_nop 11
	v_add_u32_e32 v159, s76, v152
	ds_read_b64_tr_b16 v[74:75], v159 offset:0
	ds_read_b64_tr_b16 v[76:77], v159 offset:0x1000
	ds_read_b64_tr_b16 v[66:67], v159 offset:0x2000
	ds_read_b64_tr_b16 v[68:69], v159 offset:0x3000
	v_add_u32_e32 v158, s76, v153
	ds_read_b64_tr_b16 v[78:79], v158 offset:0
	ds_read_b64_tr_b16 v[80:81], v158 offset:0x1000
	ds_read_b64_tr_b16 v[70:71], v158 offset:0x2000
	v_pk_add_f32 v[84:85], v[216:217], v[200:201]
	v_pk_add_f32 v[82:83], v[218:219], v[202:203]
	ds_read_b64_tr_b16 v[72:73], v158 offset:0x3000
	v_pk_add_f32 v[172:173], v[206:207], v[190:191]
	v_pk_add_f32 v[170:171], v[208:209], v[192:193]
	v_pk_add_f32 v[164:165], v[210:211], v[194:195]
	v_pk_add_f32 v[162:163], v[212:213], v[196:197]
	v_pk_add_f32 v[160:161], v[214:215], v[198:199]
	v_pk_add_f32 v[174:175], v[204:205], v[188:189]
	v_pk_mul_f32 v[88:89], v[88:89], v[82:83]
	v_pk_mul_f32 v[86:87], v[86:87], v[84:85]
	v_pk_mul_f32 v[84:85], v[166:167], v[160:161]
	v_pk_mul_f32 v[82:83], v[134:135], v[162:163]
	v_pk_mul_f32 v[134:135], v[132:133], v[164:165]
	v_pk_mul_f32 v[132:133], v[92:93], v[170:171]
	v_pk_mul_f32 v[92:93], v[90:91], v[172:173]
	v_pk_mul_f32 v[90:91], v[168:169], v[174:175]
	v_cmp_eq_u32_e32 vcc, 0, v157
	s_and_saveexec_b64 s[0:1], vcc
	s_cbranch_execz .LBB1_1
	v_cndmask_b32_e64 v90, 0, v90, s[8:9]
	v_cndmask_b32_e64 v91, 0, v91, s[10:11]
	v_cndmask_b32_e64 v92, v92, 0, s[34:35]
	v_cndmask_b32_e64 v93, v93, 0, s[36:37]
	v_cndmask_b32_e64 v132, v132, 0, s[4:5]
	v_cndmask_b32_e64 v133, v133, 0, s[6:7]
	v_cndmask_b32_e64 v134, v134, 0, s[12:13]
	v_cndmask_b32_e64 v135, v135, 0, s[14:15]
	v_cndmask_b32_e64 v82, v82, 0, s[16:17]
	v_cndmask_b32_e64 v83, v83, 0, s[18:19]
	v_cndmask_b32_e64 v84, v84, 0, s[20:21]
	v_cndmask_b32_e64 v85, v85, 0, s[22:23]
	v_cndmask_b32_e64 v86, v86, 0, s[24:25]
	v_cndmask_b32_e64 v87, v87, 0, s[26:27]
	v_cndmask_b32_e64 v88, v88, 0, s[28:29]
	v_cndmask_b32_e64 v89, v89, 0, s[30:31]
	s_branch .LBB1_1

	.amdhsa_kernel _Z8ret_fastPKtS0_S0_S0_PKfS2_Pt
		.amdhsa_group_segment_fixed_size 0
		.amdhsa_private_segment_fixed_size 0
		.amdhsa_kernarg_size 56
		.amdhsa_user_sgpr_count 2
		.amdhsa_user_sgpr_dispatch_ptr 0
		.amdhsa_user_sgpr_queue_ptr 0
		.amdhsa_user_sgpr_kernarg_segment_ptr 1
		.amdhsa_user_sgpr_dispatch_id 0
		.amdhsa_user_sgpr_kernarg_preload_length 0
		.amdhsa_user_sgpr_kernarg_preload_offset 0
		.amdhsa_user_sgpr_private_segment_size 0
		.amdhsa_uses_dynamic_stack 0
		.amdhsa_enable_private_segment 0
		.amdhsa_system_sgpr_workgroup_id_x 1
		.amdhsa_system_sgpr_workgroup_id_y 0
		.amdhsa_system_sgpr_workgroup_id_z 0
		.amdhsa_system_sgpr_workgroup_info 0
		.amdhsa_system_vgpr_workitem_id 0
		.amdhsa_next_free_vgpr 348
		.amdhsa_next_free_sgpr 79
		.amdhsa_accum_offset 220
		.amdhsa_reserve_vcc 1
		.amdhsa_float_round_mode_32 0
		.amdhsa_float_round_mode_16_64 0
		.amdhsa_float_denorm_mode_32 3
		.amdhsa_float_denorm_mode_16_64 3
		.amdhsa_dx10_clamp 1
		.amdhsa_ieee_mode 1
		.amdhsa_fp16_overflow 0
		.amdhsa_tg_split 0
		.amdhsa_exception_fp_ieee_invalid_op 0
		.amdhsa_exception_fp_denorm_src 0
		.amdhsa_exception_fp_ieee_div_zero 0
		.amdhsa_exception_fp_ieee_overflow 0
		.amdhsa_exception_fp_ieee_underflow 0
		.amdhsa_exception_fp_ieee_inexact 0
		.amdhsa_exception_int_div_zero 0
	.end_amdhsa_kernel

amdhsa.kernels:
  - .agpr_count:     0
    .args:
      - .offset:         0
        .size:           336
        .value_kind:     by_value
      - .offset:         336
        .size:           4
        .value_kind:     by_value
    .group_segment_fixed_size: 32768
    .kernarg_segment_align: 8
    .kernarg_segment_size: 340
    .language:       OpenCL C
    .language_version:
      - 2
      - 0
    .max_flat_workgroup_size: 256
    .name:           _Z12wconv_kernel5WDesci
    .private_segment_fixed_size: 0
    .sgpr_count:     36
    .sgpr_spill_count: 0
    .symbol:         _Z12wconv_kernel5WDesci.kd
    .uniform_work_group_size: 1
    .uses_dynamic_stack: false
    .vgpr_count:     87
    .vgpr_spill_count: 0
    .wavefront_size: 64
  - .agpr_count:     128
    .args:
      - .actual_access:  read_only
        .address_space:  global
        .offset:         0
        .size:           8
        .value_kind:     global_buffer
      - .address_space:  global
        .offset:         8
        .size:           8
        .value_kind:     global_buffer
      - .address_space:  global
        .offset:         16
        .size:           8
        .value_kind:     global_buffer
      - .actual_access:  read_only
        .address_space:  global
        .offset:         24
        .size:           8
        .value_kind:     global_buffer
      - .actual_access:  read_only
        .address_space:  global
        .offset:         32
        .size:           8
        .value_kind:     global_buffer
      - .actual_access:  read_only
        .address_space:  global
        .offset:         40
        .size:           8
        .value_kind:     global_buffer
      - .actual_access:  write_only
        .address_space:  global
        .offset:         48
        .size:           8
        .value_kind:     global_buffer
    .group_segment_fixed_size: 0
    .kernarg_segment_align: 8
    .kernarg_segment_size: 56
    .language:       OpenCL C
    .language_version:
      - 2
      - 0
    .max_flat_workgroup_size: 256
    .name:           _Z8ret_fastPKtS0_S0_S0_PKfS2_Pt
    .private_segment_fixed_size: 0
    .sgpr_count:     85
    .sgpr_spill_count: 0
    .symbol:         _Z8ret_fastPKtS0_S0_S0_PKfS2_Pt.kd
    .uniform_work_group_size: 1
    .uses_dynamic_stack: false
    .vgpr_count:     348
    .vgpr_spill_count: 0
    .wavefront_size: 64
  - .agpr_count:     0
    .args:
      - .actual_access:  read_only
        .address_space:  global
        .offset:         0
        .size:           8
        .value_kind:     global_buffer
      - .actual_access:  read_only
        .address_space:  global
        .offset:         8
        .size:           8
        .value_kind:     global_buffer
      - .actual_access:  read_only
        .address_space:  global
        .offset:         16
        .size:           8
        .value_kind:     global_buffer
      - .actual_access:  read_only
        .address_space:  global
        .offset:         24
        .size:           8
        .value_kind:     global_buffer
      - .actual_access:  write_only
        .address_space:  global
        .offset:         32
        .size:           8
        .value_kind:     global_buffer
      - .actual_access:  write_only
        .address_space:  global
        .offset:         40
        .size:           8
        .value_kind:     global_buffer
      - .actual_access:  read_only
        .address_space:  global
        .offset:         48
        .size:           8
        .value_kind:     global_buffer
      - .actual_access:  read_only
        .address_space:  global
        .offset:         56
        .size:           8
        .value_kind:     global_buffer
    .group_segment_fixed_size: 16
    .kernarg_segment_align: 8
    .kernarg_segment_size: 64
    .language:       OpenCL C
    .language_version:
      - 2
      - 0
    .max_flat_workgroup_size: 256
    .name:           _Z9ln_kernelILb0ELb0EEvPKvPKtS3_PKfPvPtS5_S5_
    .private_segment_fixed_size: 0
    .sgpr_count:     34
    .sgpr_spill_count: 0
    .symbol:         _Z9ln_kernelILb0ELb0EEvPKvPKtS3_PKfPvPtS5_S5_.kd
    .uniform_work_group_size: 1
    .uses_dynamic_stack: false
    .vgpr_count:     62
    .vgpr_spill_count: 0
    .wavefront_size: 64
  - .agpr_count:     0
    .args:
      - .actual_access:  read_only
        .address_space:  global
        .offset:         0
        .size:           8
        .value_kind:     global_buffer
      - .actual_access:  read_only
        .address_space:  global
        .offset:         8
        .size:           8
        .value_kind:     global_buffer
      - .actual_access:  read_only
        .address_space:  global
        .offset:         16
        .size:           8
        .value_kind:     global_buffer
      - .actual_access:  read_only
        .address_space:  global
        .offset:         24
        .size:           8
        .value_kind:     global_buffer
      - .actual_access:  write_only
        .address_space:  global
        .offset:         32
        .size:           8
        .value_kind:     global_buffer
      - .actual_access:  write_only
        .address_space:  global
        .offset:         40
        .size:           8
        .value_kind:     global_buffer
      - .actual_access:  read_only
        .address_space:  global
        .offset:         48
        .size:           8
        .value_kind:     global_buffer
      - .actual_access:  read_only
        .address_space:  global
        .offset:         56
        .size:           8
        .value_kind:     global_buffer
    .group_segment_fixed_size: 16
    .kernarg_segment_align: 8
    .kernarg_segment_size: 64
    .language:       OpenCL C
    .language_version:
      - 2
      - 0
    .max_flat_workgroup_size: 256
    .name:           _Z9ln_kernelILb1ELb1EEvPKvPKtS3_PKfPvPtS5_S5_
    .private_segment_fixed_size: 0
    .sgpr_count:     34
    .sgpr_spill_count: 0
    .symbol:         _Z9ln_kernelILb1ELb1EEvPKvPKtS3_PKfPvPtS5_S5_.kd
    .uniform_work_group_size: 1
    .uses_dynamic_stack: false
    .vgpr_count:     62
    .vgpr_spill_count: 0
    .wavefront_size: 64
  - .agpr_count:     0
    .args:
      - .address_space:  global
        .offset:         0
        .size:           8
        .value_kind:     global_buffer
      - .address_space:  global
        .offset:         8
        .size:           8
        .value_kind:     global_buffer
      - .offset:         16
        .size:           4
        .value_kind:     by_value
      - .offset:         20
        .size:           4
        .value_kind:     by_value
      - .offset:         24
        .size:           4
        .value_kind:     by_value
      - .offset:         28
        .size:           4
        .value_kind:     by_value
      - .offset:         32
        .size:           40
        .value_kind:     by_value
      - .offset:         72
        .size:           4
        .value_kind:     hidden_block_count_x
      - .offset:         76
        .size:           4
        .value_kind:     hidden_block_count_y
      - .offset:         80
        .size:           4
        .value_kind:     hidden_block_count_z
      - .offset:         84
        .size:           2
        .value_kind:     hidden_group_size_x
      - .offset:         86
        .size:           2
        .value_kind:     hidden_group_size_y
      - .offset:         88
        .size:           2
        .value_kind:     hidden_group_size_z
      - .offset:         90
        .size:           2
        .value_kind:     hidden_remainder_x
      - .offset:         92
        .size:           2
        .value_kind:     hidden_remainder_y
      - .offset:         94
        .size:           2
        .value_kind:     hidden_remainder_z
      - .offset:         112
        .size:           8
        .value_kind:     hidden_global_offset_x
      - .offset:         120
        .size:           8
        .value_kind:     hidden_global_offset_y
      - .offset:         128
        .size:           8
        .value_kind:     hidden_global_offset_z
      - .offset:         136
        .size:           2
        .value_kind:     hidden_grid_dims
      - .offset:         192
        .size:           4
        .value_kind:     hidden_dynamic_lds_size
    .group_segment_fixed_size: 0
    .kernarg_segment_align: 8
    .kernarg_segment_size: 328
    .language:       OpenCL C
    .language_version:
      - 2
      - 0
    .max_flat_workgroup_size: 512
    .name:           _Z9gemm_fastILi0ELi2EEvPKtS1_iiii7EpiArgs
    .private_segment_fixed_size: 0
    .sgpr_count:     55
    .sgpr_spill_count: 0
    .symbol:         _Z9gemm_fastILi0ELi2EEvPKtS1_iiii7EpiArgs.kd
    .uniform_work_group_size: 1
    .uses_dynamic_stack: false
    .vgpr_count:     255
    .vgpr_spill_count: 0
    .wavefront_size: 64
  - .agpr_count:     0
    .args:
      - .address_space:  global
        .offset:         0
        .size:           8
        .value_kind:     global_buffer
      - .address_space:  global
        .offset:         8
        .size:           8
        .value_kind:     global_buffer
      - .offset:         16
        .size:           4
        .value_kind:     by_value
      - .offset:         20
        .size:           4
        .value_kind:     by_value
      - .offset:         24
        .size:           4
        .value_kind:     by_value
      - .offset:         28
        .size:           4
        .value_kind:     by_value
      - .offset:         32
        .size:           40
        .value_kind:     by_value
    .group_segment_fixed_size: 0
    .kernarg_segment_align: 8
    .kernarg_segment_size: 72
    .language:       OpenCL C
    .language_version:
      - 2
      - 0
    .max_flat_workgroup_size: 512
    .name:           _Z9gemm_fastILi1ELi1EEvPKtS1_iiii7EpiArgs
    .private_segment_fixed_size: 0
    .sgpr_count:     32
    .sgpr_spill_count: 0
    .symbol:         _Z9gemm_fastILi1ELi1EEvPKtS1_iiii7EpiArgs.kd
    .uniform_work_group_size: 1
    .uses_dynamic_stack: false
    .vgpr_count:     247
    .vgpr_spill_count: 0
    .wavefront_size: 64
  - .agpr_count:     0
    .args:
      - .actual_access:  read_only
        .address_space:  global
        .offset:         0
        .size:           8
        .value_kind:     global_buffer
      - .actual_access:  read_only
        .address_space:  global
        .offset:         8
        .size:           8
        .value_kind:     global_buffer
      - .actual_access:  read_only
        .address_space:  global
        .offset:         16
        .size:           8
        .value_kind:     global_buffer
      - .actual_access:  read_only
        .address_space:  global
        .offset:         24
        .size:           8
        .value_kind:     global_buffer
      - .actual_access:  write_only
        .address_space:  global
        .offset:         32
        .size:           8
        .value_kind:     global_buffer
      - .actual_access:  write_only
        .address_space:  global
        .offset:         40
        .size:           8
        .value_kind:     global_buffer
      - .actual_access:  read_only
        .address_space:  global
        .offset:         48
        .size:           8
        .value_kind:     global_buffer
      - .actual_access:  read_only
        .address_space:  global
        .offset:         56
        .size:           8
        .value_kind:     global_buffer
    .group_segment_fixed_size: 16
    .kernarg_segment_align: 8
    .kernarg_segment_size: 64
    .language:       OpenCL C
    .language_version:
      - 2
      - 0
    .max_flat_workgroup_size: 256
    .name:           _Z9ln_kernelILb0ELb1EEvPKvPKtS3_PKfPvPtS5_S5_
    .private_segment_fixed_size: 0
    .sgpr_count:     34
    .sgpr_spill_count: 0
    .symbol:         _Z9ln_kernelILb0ELb1EEvPKvPKtS3_PKfPvPtS5_S5_.kd
    .uniform_work_group_size: 1
    .uses_dynamic_stack: false
    .vgpr_count:     62
    .vgpr_spill_count: 0
    .wavefront_size: 64
  - .agpr_count:     0
    .args:
      - .address_space:  global
        .offset:         0
        .size:           8
        .value_kind:     global_buffer
      - .address_space:  global
        .offset:         8
        .size:           8
        .value_kind:     global_buffer
      - .offset:         16
        .size:           4
        .value_kind:     by_value
      - .offset:         20
        .size:           4
        .value_kind:     by_value
      - .offset:         24
        .size:           4
        .value_kind:     by_value
      - .offset:         28
        .size:           4
        .value_kind:     by_value
      - .offset:         32
        .size:           40
        .value_kind:     by_value
      - .offset:         72
        .size:           4
        .value_kind:     hidden_block_count_x
      - .offset:         76
        .size:           4
        .value_kind:     hidden_block_count_y
      - .offset:         80
        .size:           4
        .value_kind:     hidden_block_count_z
      - .offset:         84
        .size:           2
        .value_kind:     hidden_group_size_x
      - .offset:         86
        .size:           2
        .value_kind:     hidden_group_size_y
      - .offset:         88
        .size:           2
        .value_kind:     hidden_group_size_z
      - .offset:         90
        .size:           2
        .value_kind:     hidden_remainder_x
      - .offset:         92
        .size:           2
        .value_kind:     hidden_remainder_y
      - .offset:         94
        .size:           2
        .value_kind:     hidden_remainder_z
      - .offset:         112
        .size:           8
        .value_kind:     hidden_global_offset_x
      - .offset:         120
        .size:           8
        .value_kind:     hidden_global_offset_y
      - .offset:         128
        .size:           8
        .value_kind:     hidden_global_offset_z
      - .offset:         136
        .size:           2
        .value_kind:     hidden_grid_dims
      - .offset:         192
        .size:           4
        .value_kind:     hidden_dynamic_lds_size
    .group_segment_fixed_size: 0
    .kernarg_segment_align: 8
    .kernarg_segment_size: 328
    .language:       OpenCL C
    .language_version:
      - 2
      - 0
    .max_flat_workgroup_size: 512
    .name:           _Z9gemm_fastILi2ELi2EEvPKtS1_iiii7EpiArgs
    .private_segment_fixed_size: 0
    .sgpr_count:     53
    .sgpr_spill_count: 0
    .symbol:         _Z9gemm_fastILi2ELi2EEvPKtS1_iiii7EpiArgs.kd
    .uniform_work_group_size: 1
    .uses_dynamic_stack: false
    .vgpr_count:     248
    .vgpr_spill_count: 0
    .wavefront_size: 64
  - .agpr_count:     0
    .args:
      - .actual_access:  read_only
        .address_space:  global
        .offset:         0
        .size:           8
        .value_kind:     global_buffer
      - .actual_access:  read_only
        .address_space:  global
        .offset:         8
        .size:           8
        .value_kind:     global_buffer
      - .actual_access:  read_only
        .address_space:  global
        .offset:         16
        .size:           8
        .value_kind:     global_buffer
      - .actual_access:  read_only
        .address_space:  global
        .offset:         24
        .size:           8
        .value_kind:     global_buffer
      - .actual_access:  write_only
        .address_space:  global
        .offset:         32
        .size:           8
        .value_kind:     global_buffer
      - .actual_access:  write_only
        .address_space:  global
        .offset:         40
        .size:           8
        .value_kind:     global_buffer
      - .actual_access:  read_only
        .address_space:  global
        .offset:         48
        .size:           8
        .value_kind:     global_buffer
      - .actual_access:  read_only
        .address_space:  global
        .offset:         56
        .size:           8
        .value_kind:     global_buffer
    .group_segment_fixed_size: 16
    .kernarg_segment_align: 8
    .kernarg_segment_size: 64
    .language:       OpenCL C
    .language_version:
      - 2
      - 0
    .max_flat_workgroup_size: 256
    .name:           _Z9ln_kernelILb1ELb0EEvPKvPKtS3_PKfPvPtS5_S5_
    .private_segment_fixed_size: 0
    .sgpr_count:     34
    .sgpr_spill_count: 0
    .symbol:         _Z9ln_kernelILb1ELb0EEvPKvPKtS3_PKfPvPtS5_S5_.kd
    .uniform_work_group_size: 1
    .uses_dynamic_stack: false
    .vgpr_count:     62
    .vgpr_spill_count: 0
    .wavefront_size: 64
